# stack13 = stack11 with the small QKV column pass requesting its weight fragments 8 k-steps ahead (8 register pairs) instead of 3, last 8 k-steps peeled
# baseline (speedup 1.0000x reference)
; #define LOADP(i_, ks_) do { pa[i_] = *(const bf16x8*)(wb + (size_t)((ks_) * 144) * 1024 + voff); pb[i_] = *(const bf16x8*)(wb + (size_t)((ks_) * 144 + 2) * 1024 + voff); } while (0)
; #define STEP(i_, ks_) do { _Pragma("unroll") for (int mi = 0; mi < 4; ++mi) { const bf16x8 f = AFRAG(mi, ks_); \
;         acc[0][mi] = __builtin_amdgcn_mfma_f32_16x16x32_bf16(pa[i_], f, acc[0][mi], 0, 0, 0); acc[1][mi] = __builtin_amdgcn_mfma_f32_16x16x32_bf16(pb[i_], f, acc[1][mi], 0, 0, 0); } } while (0)
; DEVINL void phase2(const Params& P, unsigned char* smem, XPre& X, const bool have_pre) {
;     ...
;             const int slot = 32 + (wv >> 1), fr0 = wv & 1;
;             const unsigned char* wb = (const unsigned char*)(P.ws + WS_WQF) + (size_t)(4 * slot + fr0) * 1024;
;             bf16x8 pa[4], pb[4];
;     ...
;             LOADP(0, 0); LOADP(1, 1); LOADP(2, 2);
; #pragma unroll 1
;             for (int ks = 0; ks < 32; ks += 4) {
;                 LOADP(3, ks + 3);                            __builtin_amdgcn_sched_barrier(0);
;                 STEP(0, ks);     __builtin_amdgcn_sched_barrier(0); LOADP(0, ks + 4 < 32 ? ks + 4 : 31); __builtin_amdgcn_sched_barrier(0);
;                 STEP(1, ks + 1); __builtin_amdgcn_sched_barrier(0); LOADP(1, ks + 5 < 32 ? ks + 5 : 31); __builtin_amdgcn_sched_barrier(0);
;                 STEP(2, ks + 2); __builtin_amdgcn_sched_barrier(0); LOADP(2, ks + 6 < 32 ? ks + 6 : 31); __builtin_amdgcn_sched_barrier(0);
;                 STEP(3, ks + 3); __builtin_amdgcn_sched_barrier(0);
;             }
.LBB0_191:
	v_sub_co_u32_e64 v2, s[0:1], s85, 1
	s_and_b64 s[0:1], s[0:1], exec
	v_readfirstlane_b32 s0, v2
	s_cselect_b32 s6, 2, s0
	s_and_b64 s[0:1], s[20:21], exec
	s_cselect_b32 s8, s85, s6
	s_cmp_gt_i32 s8, 1
	s_mov_b64 s[0:1], -1
	s_cbranch_scc0 .LBB0_203
	global_load_dwordx4 v[38:41], v[184:185], off
	global_load_dwordx4 v[42:45], v[184:185], off offset:2048
	s_mov_b32 s18, 0x24000
	v_lshl_add_u64 v[140:141], v[184:185], 0, s[18:19]
	global_load_dwordx4 v[18:21], v[140:141], off
	global_load_dwordx4 v[22:25], v[140:141], off offset:2048
	s_mov_b32 s18, 0x48000
	v_lshl_add_u64 v[140:141], v[184:185], 0, s[18:19]
	global_load_dwordx4 v[26:29], v[140:141], off
	global_load_dwordx4 v[34:37], v[140:141], off offset:2048
	s_mov_b32 s18, 0x6c000
	v_lshl_add_u64 v[140:141], v[184:185], 0, s[18:19]
	global_load_dwordx4 v[60:63], v[140:141], off
	global_load_dwordx4 v[64:67], v[140:141], off offset:2048
	s_mov_b32 s18, 0x90000
	v_lshl_add_u64 v[140:141], v[184:185], 0, s[18:19]
	global_load_dwordx4 v[106:109], v[140:141], off
	global_load_dwordx4 v[110:113], v[140:141], off offset:2048
	s_mov_b32 s18, 0xb4000
	v_lshl_add_u64 v[140:141], v[184:185], 0, s[18:19]
	global_load_dwordx4 v[114:117], v[140:141], off
	global_load_dwordx4 v[118:121], v[140:141], off offset:2048
	s_mov_b32 s18, 0xd8000
	v_lshl_add_u64 v[140:141], v[184:185], 0, s[18:19]
	global_load_dwordx4 v[122:125], v[140:141], off
	global_load_dwordx4 v[126:129], v[140:141], off offset:2048
	s_mov_b32 s18, 0xfc000
	v_lshl_add_u64 v[140:141], v[184:185], 0, s[18:19]
	global_load_dwordx4 v[130:133], v[140:141], off
	global_load_dwordx4 v[134:137], v[140:141], off offset:2048
	v_mov_b32_e32 v2, 0
	s_mov_b32 s6, 0
	s_mov_b64 s[0:1], 0
	v_mov_b32_e32 v58, v216
	v_mov_b32_e32 v3, v2
	v_mov_b32_e32 v4, v2
	v_mov_b32_e32 v5, v2
	v_mov_b32_e32 v10, v2
	v_mov_b32_e32 v11, v2
	v_mov_b32_e32 v12, v2
	v_mov_b32_e32 v13, v2
	v_mov_b32_e32 v30, v2
	v_mov_b32_e32 v31, v2
	v_mov_b32_e32 v32, v2
	v_mov_b32_e32 v33, v2
	v_mov_b32_e32 v50, v2
	v_mov_b32_e32 v51, v2
	v_mov_b32_e32 v52, v2
	v_mov_b32_e32 v53, v2
	v_mov_b32_e32 v6, v2
	v_mov_b32_e32 v7, v2
	v_mov_b32_e32 v8, v2
	v_mov_b32_e32 v9, v2
	v_mov_b32_e32 v14, v2
	v_mov_b32_e32 v15, v2
	v_mov_b32_e32 v16, v2
	v_mov_b32_e32 v17, v2
	v_mov_b32_e32 v46, v2
	v_mov_b32_e32 v47, v2
	v_mov_b32_e32 v48, v2
	v_mov_b32_e32 v49, v2
	v_mov_b32_e32 v54, v2
	v_mov_b32_e32 v55, v2
	v_mov_b32_e32 v56, v2
	v_mov_b32_e32 v57, v2
	s_mov_b32 s7, 0
	v_add_u32_e32 v104, -8, v58
	v_xor_b32_e32 v104, v104, v181
	v_lshl_add_u32 v104, v104, 4, v212
	v_add_u32_e32 v105, 0x10000, v104
	ds_read_b128 v[68:71], v104
	ds_read_b128 v[72:75], v104 offset:32768
	ds_read_b128 v[76:79], v105
	ds_read_b128 v[80:83], v105 offset:32768
.LBB0_193:
	v_add_u32_e32 v104, -4, v58
	v_xor_b32_e32 v104, v104, v181
	v_lshl_add_u32 v104, v104, 4, v212
	v_add_u32_e32 v105, 0x10000, v104
	ds_read_b128 v[86:89], v104
	ds_read_b128 v[90:93], v104 offset:32768
	ds_read_b128 v[94:97], v105
	ds_read_b128 v[98:101], v105 offset:32768
	s_waitcnt vmcnt(15) lgkmcnt(7)
	v_mfma_f32_16x16x32_bf16 v[54:57], v[38:41], v[68:71], v[54:57]
	s_waitcnt vmcnt(14)
	v_mfma_f32_16x16x32_bf16 v[50:53], v[42:45], v[68:71], v[50:53]
	s_waitcnt lgkmcnt(6)
	v_mfma_f32_16x16x32_bf16 v[46:49], v[38:41], v[72:75], v[46:49]
	v_mfma_f32_16x16x32_bf16 v[30:33], v[42:45], v[72:75], v[30:33]
	s_waitcnt lgkmcnt(5)
	v_mfma_f32_16x16x32_bf16 v[14:17], v[38:41], v[76:79], v[14:17]
	v_mfma_f32_16x16x32_bf16 v[10:13], v[42:45], v[76:79], v[10:13]
	s_waitcnt lgkmcnt(4)
	v_mfma_f32_16x16x32_bf16 v[6:9], v[38:41], v[80:83], v[6:9]
	v_mfma_f32_16x16x32_bf16 v[2:5], v[42:45], v[80:83], v[2:5]
	s_add_i32 s18, s7, 0x120000
	v_lshl_add_u64 v[140:141], v[184:185], 0, s[18:19]
	global_load_dwordx4 v[38:41], v[140:141], off
	global_load_dwordx4 v[42:45], v[140:141], off offset:2048
	v_xor_b32_e32 v104, v58, v181
	v_lshl_add_u32 v104, v104, 4, v212
	v_add_u32_e32 v105, 0x10000, v104
	ds_read_b128 v[68:71], v104
	ds_read_b128 v[72:75], v104 offset:32768
	ds_read_b128 v[76:79], v105
	ds_read_b128 v[80:83], v105 offset:32768
	s_waitcnt vmcnt(15) lgkmcnt(7)
	v_mfma_f32_16x16x32_bf16 v[54:57], v[18:21], v[86:89], v[54:57]
	s_waitcnt vmcnt(14)
	v_mfma_f32_16x16x32_bf16 v[50:53], v[22:25], v[86:89], v[50:53]
	s_waitcnt lgkmcnt(6)
	v_mfma_f32_16x16x32_bf16 v[46:49], v[18:21], v[90:93], v[46:49]
	v_mfma_f32_16x16x32_bf16 v[30:33], v[22:25], v[90:93], v[30:33]
	s_waitcnt lgkmcnt(5)
	v_mfma_f32_16x16x32_bf16 v[14:17], v[18:21], v[94:97], v[14:17]
	v_mfma_f32_16x16x32_bf16 v[10:13], v[22:25], v[94:97], v[10:13]
	s_waitcnt lgkmcnt(4)
	v_mfma_f32_16x16x32_bf16 v[6:9], v[18:21], v[98:101], v[6:9]
	v_mfma_f32_16x16x32_bf16 v[2:5], v[22:25], v[98:101], v[2:5]
	s_add_i32 s18, s7, 0x144000
	v_lshl_add_u64 v[140:141], v[184:185], 0, s[18:19]
	global_load_dwordx4 v[18:21], v[140:141], off
	global_load_dwordx4 v[22:25], v[140:141], off offset:2048
	v_add_u32_e32 v104, 4, v58
	v_xor_b32_e32 v104, v104, v181
	v_lshl_add_u32 v104, v104, 4, v212
	v_add_u32_e32 v105, 0x10000, v104
	ds_read_b128 v[86:89], v104
	ds_read_b128 v[90:93], v104 offset:32768
	ds_read_b128 v[94:97], v105
	ds_read_b128 v[98:101], v105 offset:32768
	s_waitcnt vmcnt(15) lgkmcnt(7)
	v_mfma_f32_16x16x32_bf16 v[54:57], v[26:29], v[68:71], v[54:57]
	s_waitcnt vmcnt(14)
	v_mfma_f32_16x16x32_bf16 v[50:53], v[34:37], v[68:71], v[50:53]
	s_waitcnt lgkmcnt(6)
	v_mfma_f32_16x16x32_bf16 v[46:49], v[26:29], v[72:75], v[46:49]
	v_mfma_f32_16x16x32_bf16 v[30:33], v[34:37], v[72:75], v[30:33]
	s_waitcnt lgkmcnt(5)
	v_mfma_f32_16x16x32_bf16 v[14:17], v[26:29], v[76:79], v[14:17]
	v_mfma_f32_16x16x32_bf16 v[10:13], v[34:37], v[76:79], v[10:13]
	s_waitcnt lgkmcnt(4)
; #define LOADP(i_, ks_) do { pa[i_] = *(const bf16x8*)(wb + (size_t)((ks_) * 144) * 1024 + voff); pb[i_] = *(const bf16x8*)(wb + (size_t)((ks_) * 144 + 2) * 1024 + voff); } while (0)
; #define STEP(i_, ks_) do { _Pragma("unroll") for (int mi = 0; mi < 4; ++mi) { const bf16x8 f = AFRAG(mi, ks_); \
;         acc[0][mi] = __builtin_amdgcn_mfma_f32_16x16x32_bf16(pa[i_], f, acc[0][mi], 0, 0, 0); acc[1][mi] = __builtin_amdgcn_mfma_f32_16x16x32_bf16(pb[i_], f, acc[1][mi], 0, 0, 0); } } while (0)
; DEVINL void phase2(const Params& P, unsigned char* smem, XPre& X, const bool have_pre) {
;     ...
;             LOADP(0, 0); LOADP(1, 1); LOADP(2, 2);
; #pragma unroll 1
;             for (int ks = 0; ks < 32; ks += 4) {
;                 LOADP(3, ks + 3);                            __builtin_amdgcn_sched_barrier(0);
;                 STEP(0, ks);     __builtin_amdgcn_sched_barrier(0); LOADP(0, ks + 4 < 32 ? ks + 4 : 31); __builtin_amdgcn_sched_barrier(0);
;                 STEP(1, ks + 1); __builtin_amdgcn_sched_barrier(0); LOADP(1, ks + 5 < 32 ? ks + 5 : 31); __builtin_amdgcn_sched_barrier(0);
;                 STEP(2, ks + 2); __builtin_amdgcn_sched_barrier(0); LOADP(2, ks + 6 < 32 ? ks + 6 : 31); __builtin_amdgcn_sched_barrier(0);
;                 STEP(3, ks + 3); __builtin_amdgcn_sched_barrier(0);
;             }
	v_mfma_f32_16x16x32_bf16 v[6:9], v[26:29], v[80:83], v[6:9]
	v_mfma_f32_16x16x32_bf16 v[2:5], v[34:37], v[80:83], v[2:5]
	s_add_i32 s18, s7, 0x168000
	v_lshl_add_u64 v[140:141], v[184:185], 0, s[18:19]
	global_load_dwordx4 v[26:29], v[140:141], off
	global_load_dwordx4 v[34:37], v[140:141], off offset:2048
	v_add_u32_e32 v104, 8, v58
	v_xor_b32_e32 v104, v104, v181
	v_lshl_add_u32 v104, v104, 4, v212
	v_add_u32_e32 v105, 0x10000, v104
	ds_read_b128 v[68:71], v104
	ds_read_b128 v[72:75], v104 offset:32768
	ds_read_b128 v[76:79], v105
	ds_read_b128 v[80:83], v105 offset:32768
	s_waitcnt vmcnt(15) lgkmcnt(7)
	v_mfma_f32_16x16x32_bf16 v[54:57], v[60:63], v[86:89], v[54:57]
	s_waitcnt vmcnt(14)
	v_mfma_f32_16x16x32_bf16 v[50:53], v[64:67], v[86:89], v[50:53]
	s_waitcnt lgkmcnt(6)
	v_mfma_f32_16x16x32_bf16 v[46:49], v[60:63], v[90:93], v[46:49]
	v_mfma_f32_16x16x32_bf16 v[30:33], v[64:67], v[90:93], v[30:33]
	s_waitcnt lgkmcnt(5)
	v_mfma_f32_16x16x32_bf16 v[14:17], v[60:63], v[94:97], v[14:17]
	v_mfma_f32_16x16x32_bf16 v[10:13], v[64:67], v[94:97], v[10:13]
	s_waitcnt lgkmcnt(4)
	v_mfma_f32_16x16x32_bf16 v[6:9], v[60:63], v[98:101], v[6:9]
	v_mfma_f32_16x16x32_bf16 v[2:5], v[64:67], v[98:101], v[2:5]
	s_add_i32 s18, s7, 0x18c000
	v_lshl_add_u64 v[140:141], v[184:185], 0, s[18:19]
	global_load_dwordx4 v[60:63], v[140:141], off
	global_load_dwordx4 v[64:67], v[140:141], off offset:2048
	v_add_u32_e32 v104, 12, v58
	v_xor_b32_e32 v104, v104, v181
	v_lshl_add_u32 v104, v104, 4, v212
	v_add_u32_e32 v105, 0x10000, v104
	ds_read_b128 v[86:89], v104
	ds_read_b128 v[90:93], v104 offset:32768
	ds_read_b128 v[94:97], v105
	ds_read_b128 v[98:101], v105 offset:32768
	s_waitcnt vmcnt(15) lgkmcnt(7)
	v_mfma_f32_16x16x32_bf16 v[54:57], v[106:109], v[68:71], v[54:57]
	s_waitcnt vmcnt(14)
	v_mfma_f32_16x16x32_bf16 v[50:53], v[110:113], v[68:71], v[50:53]
	s_waitcnt lgkmcnt(6)
	v_mfma_f32_16x16x32_bf16 v[46:49], v[106:109], v[72:75], v[46:49]
	v_mfma_f32_16x16x32_bf16 v[30:33], v[110:113], v[72:75], v[30:33]
	s_waitcnt lgkmcnt(5)
	v_mfma_f32_16x16x32_bf16 v[14:17], v[106:109], v[76:79], v[14:17]
	v_mfma_f32_16x16x32_bf16 v[10:13], v[110:113], v[76:79], v[10:13]
	s_waitcnt lgkmcnt(4)
	v_mfma_f32_16x16x32_bf16 v[6:9], v[106:109], v[80:83], v[6:9]
	v_mfma_f32_16x16x32_bf16 v[2:5], v[110:113], v[80:83], v[2:5]
	s_add_i32 s18, s7, 0x1b0000
	v_lshl_add_u64 v[140:141], v[184:185], 0, s[18:19]
	global_load_dwordx4 v[106:109], v[140:141], off
	global_load_dwordx4 v[110:113], v[140:141], off offset:2048
	v_add_u32_e32 v104, 16, v58
	v_xor_b32_e32 v104, v104, v181
	v_lshl_add_u32 v104, v104, 4, v212
	v_add_u32_e32 v105, 0x10000, v104
	ds_read_b128 v[68:71], v104
	ds_read_b128 v[72:75], v104 offset:32768
	ds_read_b128 v[76:79], v105
	ds_read_b128 v[80:83], v105 offset:32768
	s_waitcnt vmcnt(15) lgkmcnt(7)
	v_mfma_f32_16x16x32_bf16 v[54:57], v[114:117], v[86:89], v[54:57]
	s_waitcnt vmcnt(14)
	v_mfma_f32_16x16x32_bf16 v[50:53], v[118:121], v[86:89], v[50:53]
	s_waitcnt lgkmcnt(6)
	v_mfma_f32_16x16x32_bf16 v[46:49], v[114:117], v[90:93], v[46:49]
	v_mfma_f32_16x16x32_bf16 v[30:33], v[118:121], v[90:93], v[30:33]
	s_waitcnt lgkmcnt(5)
	v_mfma_f32_16x16x32_bf16 v[14:17], v[114:117], v[94:97], v[14:17]
	v_mfma_f32_16x16x32_bf16 v[10:13], v[118:121], v[94:97], v[10:13]
	s_waitcnt lgkmcnt(4)
	v_mfma_f32_16x16x32_bf16 v[6:9], v[114:117], v[98:101], v[6:9]
	v_mfma_f32_16x16x32_bf16 v[2:5], v[118:121], v[98:101], v[2:5]
	s_add_i32 s18, s7, 0x1d4000
	v_lshl_add_u64 v[140:141], v[184:185], 0, s[18:19]
	global_load_dwordx4 v[114:117], v[140:141], off
	global_load_dwordx4 v[118:121], v[140:141], off offset:2048
	v_add_u32_e32 v104, 20, v58
	v_xor_b32_e32 v104, v104, v181
	v_lshl_add_u32 v104, v104, 4, v212
	v_add_u32_e32 v105, 0x10000, v104
	ds_read_b128 v[86:89], v104
	ds_read_b128 v[90:93], v104 offset:32768
	ds_read_b128 v[94:97], v105
	ds_read_b128 v[98:101], v105 offset:32768
	s_waitcnt vmcnt(15) lgkmcnt(7)
	v_mfma_f32_16x16x32_bf16 v[54:57], v[122:125], v[68:71], v[54:57]
	s_waitcnt vmcnt(14)
	v_mfma_f32_16x16x32_bf16 v[50:53], v[126:129], v[68:71], v[50:53]
	s_waitcnt lgkmcnt(6)
	v_mfma_f32_16x16x32_bf16 v[46:49], v[122:125], v[72:75], v[46:49]
	v_mfma_f32_16x16x32_bf16 v[30:33], v[126:129], v[72:75], v[30:33]
	s_waitcnt lgkmcnt(5)
	v_mfma_f32_16x16x32_bf16 v[14:17], v[122:125], v[76:79], v[14:17]
	v_mfma_f32_16x16x32_bf16 v[10:13], v[126:129], v[76:79], v[10:13]
	s_waitcnt lgkmcnt(4)
	v_mfma_f32_16x16x32_bf16 v[6:9], v[122:125], v[80:83], v[6:9]
	v_mfma_f32_16x16x32_bf16 v[2:5], v[126:129], v[80:83], v[2:5]
	s_add_i32 s18, s7, 0x1f8000
	v_lshl_add_u64 v[140:141], v[184:185], 0, s[18:19]
	global_load_dwordx4 v[122:125], v[140:141], off
	global_load_dwordx4 v[126:129], v[140:141], off offset:2048
	v_add_u32_e32 v104, 24, v58
	v_xor_b32_e32 v104, v104, v181
	v_lshl_add_u32 v104, v104, 4, v212
	v_add_u32_e32 v105, 0x10000, v104
	ds_read_b128 v[68:71], v104
	ds_read_b128 v[72:75], v104 offset:32768
	ds_read_b128 v[76:79], v105
	ds_read_b128 v[80:83], v105 offset:32768
	s_waitcnt vmcnt(15) lgkmcnt(7)
	v_mfma_f32_16x16x32_bf16 v[54:57], v[130:133], v[86:89], v[54:57]
	s_waitcnt vmcnt(14)
	v_mfma_f32_16x16x32_bf16 v[50:53], v[134:137], v[86:89], v[50:53]
	s_waitcnt lgkmcnt(6)
	v_mfma_f32_16x16x32_bf16 v[46:49], v[130:133], v[90:93], v[46:49]
	v_mfma_f32_16x16x32_bf16 v[30:33], v[134:137], v[90:93], v[30:33]
	s_waitcnt lgkmcnt(5)
	v_mfma_f32_16x16x32_bf16 v[14:17], v[130:133], v[94:97], v[14:17]
	v_mfma_f32_16x16x32_bf16 v[10:13], v[134:137], v[94:97], v[10:13]
	s_waitcnt lgkmcnt(4)
	v_mfma_f32_16x16x32_bf16 v[6:9], v[130:133], v[98:101], v[6:9]
	v_mfma_f32_16x16x32_bf16 v[2:5], v[134:137], v[98:101], v[2:5]
	s_add_i32 s18, s7, 0x21c000
	v_lshl_add_u64 v[140:141], v[184:185], 0, s[18:19]
	global_load_dwordx4 v[130:133], v[140:141], off
	global_load_dwordx4 v[134:137], v[140:141], off offset:2048
	v_add_u32_e32 v58, 32, v58
	s_add_i32 s7, s7, 0x120000
	s_add_i32 s6, s6, 8
	s_cmp_lt_u32 s6, 24
	s_cbranch_scc1 .LBB0_193
; #define LOADP(i_, ks_) do { pa[i_] = *(const bf16x8*)(wb + (size_t)((ks_) * 144) * 1024 + voff); pb[i_] = *(const bf16x8*)(wb + (size_t)((ks_) * 144 + 2) * 1024 + voff); } while (0)
; #define STEP(i_, ks_) do { _Pragma("unroll") for (int mi = 0; mi < 4; ++mi) { const bf16x8 f = AFRAG(mi, ks_); \
;         acc[0][mi] = __builtin_amdgcn_mfma_f32_16x16x32_bf16(pa[i_], f, acc[0][mi], 0, 0, 0); acc[1][mi] = __builtin_amdgcn_mfma_f32_16x16x32_bf16(pb[i_], f, acc[1][mi], 0, 0, 0); } } while (0)
; DEVINL void phase2(const Params& P, unsigned char* smem, XPre& X, const bool have_pre) {
;     ...
;             LOADP(0, 0); LOADP(1, 1); LOADP(2, 2);
; #pragma unroll 1
;             for (int ks = 0; ks < 32; ks += 4) {
;                 LOADP(3, ks + 3);                            __builtin_amdgcn_sched_barrier(0);
;                 STEP(0, ks);     __builtin_amdgcn_sched_barrier(0); LOADP(0, ks + 4 < 32 ? ks + 4 : 31); __builtin_amdgcn_sched_barrier(0);
;                 STEP(1, ks + 1); __builtin_amdgcn_sched_barrier(0); LOADP(1, ks + 5 < 32 ? ks + 5 : 31); __builtin_amdgcn_sched_barrier(0);
;                 STEP(2, ks + 2); __builtin_amdgcn_sched_barrier(0); LOADP(2, ks + 6 < 32 ? ks + 6 : 31); __builtin_amdgcn_sched_barrier(0);
;                 STEP(3, ks + 3); __builtin_amdgcn_sched_barrier(0);
;             }
	v_add_u32_e32 v104, -4, v58
	v_xor_b32_e32 v104, v104, v181
	v_lshl_add_u32 v104, v104, 4, v212
	v_add_u32_e32 v105, 0x10000, v104
	ds_read_b128 v[86:89], v104
	ds_read_b128 v[90:93], v104 offset:32768
	ds_read_b128 v[94:97], v105
	ds_read_b128 v[98:101], v105 offset:32768
	s_waitcnt vmcnt(15) lgkmcnt(7)
	v_mfma_f32_16x16x32_bf16 v[54:57], v[38:41], v[68:71], v[54:57]
	s_waitcnt vmcnt(14)
	v_mfma_f32_16x16x32_bf16 v[50:53], v[42:45], v[68:71], v[50:53]
	s_waitcnt lgkmcnt(6)
	v_mfma_f32_16x16x32_bf16 v[46:49], v[38:41], v[72:75], v[46:49]
	v_mfma_f32_16x16x32_bf16 v[30:33], v[42:45], v[72:75], v[30:33]
	s_waitcnt lgkmcnt(5)
	v_mfma_f32_16x16x32_bf16 v[14:17], v[38:41], v[76:79], v[14:17]
	v_mfma_f32_16x16x32_bf16 v[10:13], v[42:45], v[76:79], v[10:13]
	s_waitcnt lgkmcnt(4)
	v_mfma_f32_16x16x32_bf16 v[6:9], v[38:41], v[80:83], v[6:9]
	v_mfma_f32_16x16x32_bf16 v[2:5], v[42:45], v[80:83], v[2:5]
	v_xor_b32_e32 v104, v58, v181
	v_lshl_add_u32 v104, v104, 4, v212
	v_add_u32_e32 v105, 0x10000, v104
	ds_read_b128 v[68:71], v104
	ds_read_b128 v[72:75], v104 offset:32768
	ds_read_b128 v[76:79], v105
	ds_read_b128 v[80:83], v105 offset:32768
	s_waitcnt vmcnt(13) lgkmcnt(7)
	v_mfma_f32_16x16x32_bf16 v[54:57], v[18:21], v[86:89], v[54:57]
	s_waitcnt vmcnt(12)
	v_mfma_f32_16x16x32_bf16 v[50:53], v[22:25], v[86:89], v[50:53]
	s_waitcnt lgkmcnt(6)
	v_mfma_f32_16x16x32_bf16 v[46:49], v[18:21], v[90:93], v[46:49]
	v_mfma_f32_16x16x32_bf16 v[30:33], v[22:25], v[90:93], v[30:33]
	s_waitcnt lgkmcnt(5)
	v_mfma_f32_16x16x32_bf16 v[14:17], v[18:21], v[94:97], v[14:17]
	v_mfma_f32_16x16x32_bf16 v[10:13], v[22:25], v[94:97], v[10:13]
	s_waitcnt lgkmcnt(4)
	v_mfma_f32_16x16x32_bf16 v[6:9], v[18:21], v[98:101], v[6:9]
	v_mfma_f32_16x16x32_bf16 v[2:5], v[22:25], v[98:101], v[2:5]
	v_add_u32_e32 v104, 4, v58
	v_xor_b32_e32 v104, v104, v181
	v_lshl_add_u32 v104, v104, 4, v212
	v_add_u32_e32 v105, 0x10000, v104
	ds_read_b128 v[86:89], v104
	ds_read_b128 v[90:93], v104 offset:32768
	ds_read_b128 v[94:97], v105
	ds_read_b128 v[98:101], v105 offset:32768
	s_waitcnt vmcnt(11) lgkmcnt(7)
	v_mfma_f32_16x16x32_bf16 v[54:57], v[26:29], v[68:71], v[54:57]
	s_waitcnt vmcnt(10)
	v_mfma_f32_16x16x32_bf16 v[50:53], v[34:37], v[68:71], v[50:53]
	s_waitcnt lgkmcnt(6)
	v_mfma_f32_16x16x32_bf16 v[46:49], v[26:29], v[72:75], v[46:49]
	v_mfma_f32_16x16x32_bf16 v[30:33], v[34:37], v[72:75], v[30:33]
	s_waitcnt lgkmcnt(5)
	v_mfma_f32_16x16x32_bf16 v[14:17], v[26:29], v[76:79], v[14:17]
	v_mfma_f32_16x16x32_bf16 v[10:13], v[34:37], v[76:79], v[10:13]
	s_waitcnt lgkmcnt(4)
	v_mfma_f32_16x16x32_bf16 v[6:9], v[26:29], v[80:83], v[6:9]
	v_mfma_f32_16x16x32_bf16 v[2:5], v[34:37], v[80:83], v[2:5]
	v_add_u32_e32 v104, 8, v58
	v_xor_b32_e32 v104, v104, v181
	v_lshl_add_u32 v104, v104, 4, v212
	v_add_u32_e32 v105, 0x10000, v104
	ds_read_b128 v[68:71], v104
	ds_read_b128 v[72:75], v104 offset:32768
	ds_read_b128 v[76:79], v105
	ds_read_b128 v[80:83], v105 offset:32768
	s_waitcnt vmcnt(9) lgkmcnt(7)
	v_mfma_f32_16x16x32_bf16 v[54:57], v[60:63], v[86:89], v[54:57]
	s_waitcnt vmcnt(8)
	v_mfma_f32_16x16x32_bf16 v[50:53], v[64:67], v[86:89], v[50:53]
	s_waitcnt lgkmcnt(6)
	v_mfma_f32_16x16x32_bf16 v[46:49], v[60:63], v[90:93], v[46:49]
	v_mfma_f32_16x16x32_bf16 v[30:33], v[64:67], v[90:93], v[30:33]
	s_waitcnt lgkmcnt(5)
	v_mfma_f32_16x16x32_bf16 v[14:17], v[60:63], v[94:97], v[14:17]
	v_mfma_f32_16x16x32_bf16 v[10:13], v[64:67], v[94:97], v[10:13]
	s_waitcnt lgkmcnt(4)
	v_mfma_f32_16x16x32_bf16 v[6:9], v[60:63], v[98:101], v[6:9]
	v_mfma_f32_16x16x32_bf16 v[2:5], v[64:67], v[98:101], v[2:5]
	v_add_u32_e32 v104, 12, v58
	v_xor_b32_e32 v104, v104, v181
	v_lshl_add_u32 v104, v104, 4, v212
	v_add_u32_e32 v105, 0x10000, v104
	ds_read_b128 v[86:89], v104
	ds_read_b128 v[90:93], v104 offset:32768
	ds_read_b128 v[94:97], v105
	ds_read_b128 v[98:101], v105 offset:32768
	s_waitcnt vmcnt(7) lgkmcnt(7)
	v_mfma_f32_16x16x32_bf16 v[54:57], v[106:109], v[68:71], v[54:57]
	s_waitcnt vmcnt(6)
; #define LOADP(i_, ks_) do { pa[i_] = *(const bf16x8*)(wb + (size_t)((ks_) * 144) * 1024 + voff); pb[i_] = *(const bf16x8*)(wb + (size_t)((ks_) * 144 + 2) * 1024 + voff); } while (0)
; #define STEP(i_, ks_) do { _Pragma("unroll") for (int mi = 0; mi < 4; ++mi) { const bf16x8 f = AFRAG(mi, ks_); \
;         acc[0][mi] = __builtin_amdgcn_mfma_f32_16x16x32_bf16(pa[i_], f, acc[0][mi], 0, 0, 0); acc[1][mi] = __builtin_amdgcn_mfma_f32_16x16x32_bf16(pb[i_], f, acc[1][mi], 0, 0, 0); } } while (0)
; DEVINL void qkv_store_head(const Params& P, const f32x4 (&v0)[4], int slot, int m, int g, const float* rc, const float* rs, int nfr, int fr0) {
;     ...
;     if (region == 3 || region == 4) {
; #pragma unroll
;         for (int ni = 0; ni < 2; ++ni) if (ni < hp) {
;             const int fr = fr0 + ni * fstep;
;             const f32x4 cs = *(const f32x4*)(rc + sq * 32 + 16 * fr + 4 * g), sn = *(const f32x4*)(rs + sq * 32 + 16 * fr + 4 * g);
;             const f32x4 x1 = v[ni], x2 = v[ni + hp];
;             v[ni] = x1 * cs - x2 * sn; v[ni + hp] = x2 * cs + x1 * sn;
;         }
; DEVINL void phase2(const Params& P, unsigned char* smem, XPre& X, const bool have_pre) {
;     ...
;             LOADP(0, 0); LOADP(1, 1); LOADP(2, 2);
; #pragma unroll 1
;             for (int ks = 0; ks < 32; ks += 4) {
;                 LOADP(3, ks + 3);                            __builtin_amdgcn_sched_barrier(0);
;                 STEP(0, ks);     __builtin_amdgcn_sched_barrier(0); LOADP(0, ks + 4 < 32 ? ks + 4 : 31); __builtin_amdgcn_sched_barrier(0);
;                 STEP(1, ks + 1); __builtin_amdgcn_sched_barrier(0); LOADP(1, ks + 5 < 32 ? ks + 5 : 31); __builtin_amdgcn_sched_barrier(0);
;                 STEP(2, ks + 2); __builtin_amdgcn_sched_barrier(0); LOADP(2, ks + 6 < 32 ? ks + 6 : 31); __builtin_amdgcn_sched_barrier(0);
;                 STEP(3, ks + 3); __builtin_amdgcn_sched_barrier(0);
;             }
	v_mfma_f32_16x16x32_bf16 v[50:53], v[110:113], v[68:71], v[50:53]
	s_waitcnt lgkmcnt(6)
	v_mfma_f32_16x16x32_bf16 v[46:49], v[106:109], v[72:75], v[46:49]
	v_mfma_f32_16x16x32_bf16 v[30:33], v[110:113], v[72:75], v[30:33]
	s_waitcnt lgkmcnt(5)
	v_mfma_f32_16x16x32_bf16 v[14:17], v[106:109], v[76:79], v[14:17]
	v_mfma_f32_16x16x32_bf16 v[10:13], v[110:113], v[76:79], v[10:13]
	s_waitcnt lgkmcnt(4)
	v_mfma_f32_16x16x32_bf16 v[6:9], v[106:109], v[80:83], v[6:9]
	v_mfma_f32_16x16x32_bf16 v[2:5], v[110:113], v[80:83], v[2:5]
	v_add_u32_e32 v104, 16, v58
	v_xor_b32_e32 v104, v104, v181
	v_lshl_add_u32 v104, v104, 4, v212
	v_add_u32_e32 v105, 0x10000, v104
	ds_read_b128 v[68:71], v104
	ds_read_b128 v[72:75], v104 offset:32768
	ds_read_b128 v[76:79], v105
	ds_read_b128 v[80:83], v105 offset:32768
	s_waitcnt vmcnt(5) lgkmcnt(7)
	v_mfma_f32_16x16x32_bf16 v[54:57], v[114:117], v[86:89], v[54:57]
	s_waitcnt vmcnt(4)
	v_mfma_f32_16x16x32_bf16 v[50:53], v[118:121], v[86:89], v[50:53]
	s_waitcnt lgkmcnt(6)
	v_mfma_f32_16x16x32_bf16 v[46:49], v[114:117], v[90:93], v[46:49]
	v_mfma_f32_16x16x32_bf16 v[30:33], v[118:121], v[90:93], v[30:33]
	s_waitcnt lgkmcnt(5)
	v_mfma_f32_16x16x32_bf16 v[14:17], v[114:117], v[94:97], v[14:17]
	v_mfma_f32_16x16x32_bf16 v[10:13], v[118:121], v[94:97], v[10:13]
	s_waitcnt lgkmcnt(4)
	v_mfma_f32_16x16x32_bf16 v[6:9], v[114:117], v[98:101], v[6:9]
	v_mfma_f32_16x16x32_bf16 v[2:5], v[118:121], v[98:101], v[2:5]
	v_add_u32_e32 v104, 20, v58
	v_xor_b32_e32 v104, v104, v181
	v_lshl_add_u32 v104, v104, 4, v212
	v_add_u32_e32 v105, 0x10000, v104
	ds_read_b128 v[86:89], v104
	ds_read_b128 v[90:93], v104 offset:32768
	ds_read_b128 v[94:97], v105
	ds_read_b128 v[98:101], v105 offset:32768
	s_waitcnt vmcnt(3) lgkmcnt(7)
	v_mfma_f32_16x16x32_bf16 v[54:57], v[122:125], v[68:71], v[54:57]
	s_waitcnt vmcnt(2)
	v_mfma_f32_16x16x32_bf16 v[50:53], v[126:129], v[68:71], v[50:53]
	s_waitcnt lgkmcnt(6)
	v_mfma_f32_16x16x32_bf16 v[46:49], v[122:125], v[72:75], v[46:49]
	v_mfma_f32_16x16x32_bf16 v[30:33], v[126:129], v[72:75], v[30:33]
	s_waitcnt lgkmcnt(5)
	v_mfma_f32_16x16x32_bf16 v[14:17], v[122:125], v[76:79], v[14:17]
	v_mfma_f32_16x16x32_bf16 v[10:13], v[126:129], v[76:79], v[10:13]
	s_waitcnt lgkmcnt(4)
	v_mfma_f32_16x16x32_bf16 v[6:9], v[122:125], v[80:83], v[6:9]
	v_mfma_f32_16x16x32_bf16 v[2:5], v[126:129], v[80:83], v[2:5]
	s_waitcnt vmcnt(1) lgkmcnt(3)
	v_mfma_f32_16x16x32_bf16 v[54:57], v[130:133], v[86:89], v[54:57]
	s_waitcnt vmcnt(0)
	v_mfma_f32_16x16x32_bf16 v[50:53], v[134:137], v[86:89], v[50:53]
	s_waitcnt lgkmcnt(2)
	v_mfma_f32_16x16x32_bf16 v[46:49], v[130:133], v[90:93], v[46:49]
	v_mfma_f32_16x16x32_bf16 v[30:33], v[134:137], v[90:93], v[30:33]
	s_waitcnt lgkmcnt(1)
	v_mfma_f32_16x16x32_bf16 v[14:17], v[130:133], v[94:97], v[14:17]
	v_mfma_f32_16x16x32_bf16 v[10:13], v[134:137], v[94:97], v[10:13]
	s_waitcnt lgkmcnt(0)
	v_mfma_f32_16x16x32_bf16 v[6:9], v[130:133], v[98:101], v[6:9]
	v_mfma_f32_16x16x32_bf16 v[2:5], v[134:137], v[98:101], v[2:5]
	s_waitcnt vmcnt(3)
	v_mov_b32_e32 v20, v180
	s_and_b64 vcc, s[20:21], exec
	s_waitcnt vmcnt(2)
	v_and_or_b32 v24, v20, 15, s62
	v_and_b32_e32 v18, -16, v20
	v_add_u32_e32 v22, s25, v18
	v_add_u32_e32 v23, s81, v18
	v_lshlrev_b32_e32 v178, 7, v24
	s_cbranch_vccz .LBB0_196
	v_add_u32_e32 v18, v23, v178
	s_waitcnt vmcnt(1)
	ds_read_b128 v[26:29], v18
	v_add_u32_e32 v18, v22, v178
	s_waitcnt vmcnt(0)
	ds_read_b128 v[34:37], v18
	s_waitcnt lgkmcnt(1)
	v_pk_mul_f32 v[18:19], v[52:53], v[28:29]
	v_pk_mul_f32 v[38:39], v[50:51], v[26:27]
	s_waitcnt lgkmcnt(0)
	v_pk_fma_f32 v[18:19], v[56:57], v[36:37], v[18:19] neg_lo:[0,0,1] neg_hi:[0,0,1]
	v_pk_fma_f32 v[38:39], v[54:55], v[34:35], v[38:39] neg_lo:[0,0,1] neg_hi:[0,0,1]
	v_pk_mul_f32 v[28:29], v[56:57], v[28:29]
	v_pk_mul_f32 v[26:27], v[54:55], v[26:27]
	v_pk_fma_f32 v[52:53], v[52:53], v[36:37], v[28:29]
	v_pk_fma_f32 v[50:51], v[50:51], v[34:35], v[26:27]
	v_mov_b32_e32 v54, v38
	v_mov_b32_e32 v55, v39
	v_mov_b32_e32 v56, v18
	v_mov_b32_e32 v57, v19
